# c8
# speedup vs baseline: 1.0131x; 1.0022x over previous
.LBB2_95:
	s_or_b64 exec, exec, s[34:35]
	v_mfma_f32_32x32x16_f16 v[56:71], v[168:171], v[72:75], v[56:71]
	ds_read_b128 v[218:221], v205 offset:3168
	ds_read_b128 v[222:225], v207 offset:3168
	v_mfma_f32_32x32x16_f16 v[72:87], v[176:179], v[72:75], 0
	s_waitcnt lgkmcnt(3)
	v_mfma_f32_32x32x16_f16 v[56:71], v[160:163], v[100:103], v[56:71]
	v_mfma_f32_32x32x16_f16 v[72:87], v[172:175], v[100:103], v[72:87]
	v_mfma_f32_32x32x16_f16 v[56:71], v[164:167], v[96:99], v[56:71]
	v_mfma_f32_32x32x16_f16 v[72:87], v[168:171], v[96:99], v[72:87]
	ds_read_b128 v[96:99], v205 offset:6336
	ds_read_b128 v[100:103], v207 offset:6336
	s_waitcnt lgkmcnt(4)
	v_mfma_f32_32x32x16_f16 v[56:71], v[156:159], v[92:95], v[56:71]
	v_mfma_f32_32x32x16_f16 v[72:87], v[160:163], v[92:95], v[72:87]
	v_add_f32_e32 v14, v187, v14
	v_add_f32_e32 v15, v188, v15
	v_add_f32_e32 v12, v180, v12
	v_add_f32_e32 v13, v186, v13
	s_waitcnt lgkmcnt(3)
	v_mfma_f32_32x32x16_f16 v[72:87], v[164:167], v[218:221], v[72:87]
	v_max_f32_e32 v14, 0, v14
	v_max_f32_e32 v15, 0, v15
	v_max_f32_e32 v12, 0, v12
	v_max_f32_e32 v13, 0, v13
	v_cvt_pk_f16_f32 v15, v14, v15
	v_cvt_pk_f16_f32 v14, v12, v13
	v_add_f32_e32 v12, v189, v16
	v_max_f32_e32 v16, 0, v12
	v_add_f32_e32 v12, v184, v46
	v_add_f32_e32 v13, v185, v47
	v_max_f32_e32 v12, 0, v12
	v_max_f32_e32 v13, 0, v13
	v_cvt_pk_f16_f32 v13, v12, v13
	v_add_f32_e32 v12, v182, v44
	v_add_f32_e32 v44, v183, v45
	s_waitcnt lgkmcnt(2)
	v_mfma_f32_32x32x16_f16 v[72:87], v[156:159], v[222:225], v[72:87]
	v_max_f32_e32 v12, 0, v12
	v_max_f32_e32 v44, 0, v44
	v_cvt_pk_f16_f32 v12, v12, v44
	v_add_f32_e32 v44, v181, v48
	ds_read_b128 v[92:95], v205 offset:7392
	ds_read_b128 v[226:229], v207 offset:7392
	v_add_u32_e32 v48, v1, v213
	v_max_f32_e32 v55, 0, v44
	v_add_u32_e32 v44, 32, v48
	v_ashrrev_i32_e32 v45, 31, v44
	v_permlane32_swap_b32_e32 v12, v14
	v_permlane32_swap_b32_e32 v13, v15
	v_permlane32_swap_b32_e32 v55, v16
	v_lshl_add_u64 v[46:47], v[44:45], 4, s[16:17]
	global_store_dwordx4 v[46:47], v[12:15], off sc1
	s_nop 1
	v_cvt_pk_f16_f32 v14, v55, v16
	v_lshl_add_u64 v[12:13], v[44:45], 2, s[18:19]
	global_store_dword v[12:13], v14, off sc1
	s_waitcnt lgkmcnt(3)
	v_mfma_f32_32x32x16_f16 v[56:71], v[136:139], v[96:99], v[56:71]
	ds_read_b128 v[96:99], v205 offset:8448
	ds_read_b128 v[180:183], v207 offset:8448
	s_waitcnt lgkmcnt(4)
	v_mfma_f32_32x32x16_f16 v[56:71], v[140:143], v[100:103], v[56:71]
	s_waitcnt lgkmcnt(3)
	v_mfma_f32_32x32x16_f16 v[56:71], v[120:123], v[92:95], v[56:71]
	ds_read_b128 v[12:15], v205 offset:9504
	ds_read_b128 v[44:47], v207 offset:9504
	v_mfma_f32_32x32x16_f16 v[72:87], v[136:139], v[92:95], v[72:87]
	s_waitcnt lgkmcnt(4)
	v_mfma_f32_32x32x16_f16 v[56:71], v[152:155], v[226:229], v[56:71]
	v_mfma_f32_32x32x16_f16 v[72:87], v[140:143], v[226:229], v[72:87]
	s_waitcnt lgkmcnt(3)
	v_mfma_f32_32x32x16_f16 v[56:71], v[148:151], v[96:99], v[56:71]
	v_mfma_f32_32x32x16_f16 v[72:87], v[120:123], v[96:99], v[72:87]
	ds_read_b128 v[100:103], v205 offset:12672
	ds_read_b128 v[96:99], v207 offset:12672
	s_waitcnt vmcnt(3)
	ds_write_b128 v208, v[88:91] offset:38032
	s_waitcnt vmcnt(2)
	ds_write_b32 v230, v49 offset:38564
	s_waitcnt lgkmcnt(6)
	v_mfma_f32_32x32x16_f16 v[56:71], v[144:147], v[180:183], v[56:71]
	v_mfma_f32_32x32x16_f16 v[72:87], v[152:155], v[180:183], v[72:87]
	ds_write_b32 v231, v49 offset:38552
	ds_write_b32 v232, v49 offset:38576
	s_waitcnt lgkmcnt(7)
	v_mfma_f32_32x32x16_f16 v[72:87], v[148:151], v[12:15], v[72:87]
	ds_read_b128 v[92:95], v205 offset:13728
	ds_read_b128 v[12:15], v207 offset:13728
	s_waitcnt lgkmcnt(8)
	v_mfma_f32_32x32x16_f16 v[72:87], v[144:147], v[44:47], v[72:87]
	s_waitcnt lgkmcnt(7)
	v_mfma_f32_32x32x16_f16 v[56:71], v[132:135], v[100:103], v[56:71]
	ds_read_b128 v[88:91], v205 offset:14784
	ds_read_b128 v[44:47], v207 offset:14784
	s_waitcnt lgkmcnt(8)
	v_mfma_f32_32x32x16_f16 v[56:71], v[108:111], v[96:99], v[56:71]
	s_and_saveexec_b64 s[34:35], s[0:1]
	s_cbranch_execz .LBB2_104
	ds_write_b128 v210, v[28:31] offset:38032
	ds_write_b32 v233, v23 offset:38564
	ds_write_b32 v234, v23 offset:38552
	ds_write_b32 v235, v23 offset:38576
.LBB2_104:
	s_or_b64 exec, exec, s[34:35]
	s_waitcnt lgkmcnt(7)
	v_mfma_f32_32x32x16_f16 v[56:71], v[128:131], v[92:95], v[56:71]
	v_mfma_f32_32x32x16_f16 v[72:87], v[132:135], v[92:95], v[72:87]
	ds_read_b128 v[92:95], v205 offset:15840
	ds_read_b128 v[28:31], v207 offset:15840
	s_waitcnt lgkmcnt(8)
	v_mfma_f32_32x32x16_f16 v[56:71], v[124:127], v[12:15], v[56:71]
	v_mfma_f32_32x32x16_f16 v[72:87], v[108:111], v[12:15], v[72:87]
	s_waitcnt lgkmcnt(15)
	s_and_saveexec_b64 s[34:35], s[8:9]
	s_cbranch_execz .LBB2_109
	ds_write_b128 v211, v[24:27] offset:38032
	ds_write_b32 v236, v17 offset:38564
	ds_write_b32 v237, v17 offset:38552
	ds_write_b32 v238, v17 offset:38576

.LBB2_115:
	s_or_b64 exec, exec, s[28:29]
	v_add_f32_e32 v49, v19, v40
	v_add_f32_e32 v55, v20, v41
	v_add_f32_e32 v54, v54, v11
	v_add_f32_e32 v39, v18, v39
	v_add_f32_e32 v222, v21, v42
	v_add_f32_e32 v223, v22, v43
	v_add_f32_e32 v7, v50, v7
	v_add_f32_e32 v224, v51, v8
	v_add_f32_e32 v225, v52, v9
	v_add_f32_e32 v226, v53, v10
	v_mfma_f32_32x32x16_f16 v[88:103], v[168:171], v[12:15], v[88:103]
	ds_read_b128 v[40:43], v205 offset:41184
	ds_read_b128 v[50:53], v207 offset:41184
	v_mfma_f32_32x32x16_f16 v[240:255], v[176:179], v[12:15], 0
	s_waitcnt lgkmcnt(3)
	v_mfma_f32_32x32x16_f16 v[88:103], v[160:163], v[188:191], v[88:103]
	v_mfma_f32_32x32x16_f16 v[240:255], v[172:175], v[188:191], v[240:255]
	v_mfma_f32_32x32x16_f16 v[88:103], v[164:167], v[184:187], v[88:103]
	v_mfma_f32_32x32x16_f16 v[240:255], v[168:171], v[184:187], v[240:255]
	ds_read_b128 v[184:187], v205 offset:44352
	ds_read_b128 v[188:191], v207 offset:44352
	s_waitcnt lgkmcnt(4)
	v_mfma_f32_32x32x16_f16 v[88:103], v[156:159], v[180:183], v[88:103]
	v_mfma_f32_32x32x16_f16 v[240:255], v[160:163], v[180:183], v[240:255]
	v_add_f32_e32 v84, v225, v84
	v_add_f32_e32 v85, v226, v85
	s_waitcnt lgkmcnt(3)
	v_mfma_f32_32x32x16_f16 v[240:255], v[164:167], v[40:43], v[240:255]
	v_add_f32_e32 v40, 0, v85
	v_max_f32_e32 v84, 0, v84
	v_max_f32_e32 v40, 0, v40
	v_cvt_pk_f16_f32 v43, v84, v40
	v_add_f32_e32 v7, v7, v82
	v_add_f32_e32 v40, v224, v83
	v_max_f32_e32 v7, 0, v7
	v_max_f32_e32 v40, 0, v40
	v_cvt_pk_f16_f32 v42, v7, v40
	v_add_f32_e32 v40, v55, v68
	v_add_f32_e32 v41, v222, v69
	v_max_f32_e32 v40, 0, v40
	v_max_f32_e32 v41, 0, v41
	s_waitcnt lgkmcnt(2)
	v_mfma_f32_32x32x16_f16 v[240:255], v[156:159], v[50:53], v[240:255]
	v_cvt_pk_f16_f32 v41, v40, v41
	v_add_f32_e32 v39, v39, v66
	v_add_f32_e32 v40, v49, v67
	v_max_f32_e32 v39, 0, v39
	v_max_f32_e32 v40, 0, v40
	ds_read_b128 v[180:183], v205 offset:45408
	ds_read_b128 v[218:221], v207 offset:45408
	v_add_f32_e32 v7, v54, v86
	v_cvt_pk_f16_f32 v40, v39, v40
	v_add_f32_e32 v39, v223, v70
	v_add_u32_e32 v48, 64, v48
	v_max_f32_e32 v7, 0, v7
	v_max_f32_e32 v39, 0, v39
	v_ashrrev_i32_e32 v49, 31, v48
	v_permlane32_swap_b32_e32 v40, v42
	v_permlane32_swap_b32_e32 v41, v43
	v_permlane32_swap_b32_e32 v39, v7
	v_lshl_add_u64 v[50:51], v[48:49], 4, s[16:17]
	global_store_dwordx4 v[50:51], v[40:43], off sc1
	v_cvt_pk_f16_f32 v7, v39, v7
	s_nop 0
	v_lshl_add_u64 v[40:41], v[48:49], 2, s[18:19]
	global_store_dword v[40:41], v7, off sc1
	s_waitcnt lgkmcnt(3)
	v_mfma_f32_32x32x16_f16 v[88:103], v[136:139], v[184:187], v[88:103]
	ds_read_b128 v[52:55], v205 offset:46464
	ds_read_b128 v[66:69], v207 offset:46464
	s_waitcnt lgkmcnt(4)
	v_mfma_f32_32x32x16_f16 v[88:103], v[140:143], v[188:191], v[88:103]
	s_waitcnt lgkmcnt(3)
	v_mfma_f32_32x32x16_f16 v[88:103], v[120:123], v[180:183], v[88:103]
	ds_read_b128 v[48:51], v205 offset:47520
	ds_read_b128 v[40:43], v207 offset:47520
	v_mfma_f32_32x32x16_f16 v[240:255], v[136:139], v[180:183], v[240:255]
	s_waitcnt lgkmcnt(4)
	v_mfma_f32_32x32x16_f16 v[88:103], v[152:155], v[218:221], v[88:103]
	v_mfma_f32_32x32x16_f16 v[240:255], v[140:143], v[218:221], v[240:255]
	s_waitcnt lgkmcnt(3)
	v_mfma_f32_32x32x16_f16 v[88:103], v[148:151], v[52:55], v[88:103]
	v_mfma_f32_32x32x16_f16 v[240:255], v[120:123], v[52:55], v[240:255]
	ds_read_b128 v[52:55], v205 offset:50688
	ds_read_b128 v[82:85], v207 offset:50688
	s_waitcnt vmcnt(3)
	ds_write_b128 v208, v[44:47] offset:16
	s_waitcnt vmcnt(2)
	ds_write_b32 v230, v214 offset:548
	s_waitcnt lgkmcnt(6)
	v_mfma_f32_32x32x16_f16 v[88:103], v[144:147], v[66:69], v[88:103]
	v_mfma_f32_32x32x16_f16 v[240:255], v[152:155], v[66:69], v[240:255]
	ds_write_b32 v231, v214 offset:536
	ds_write_b32 v232, v214 offset:560
	s_waitcnt lgkmcnt(7)
	v_mfma_f32_32x32x16_f16 v[240:255], v[148:151], v[48:51], v[240:255]
	ds_read_b128 v[66:69], v205 offset:51744
	ds_read_b128 v[44:47], v207 offset:51744
	s_waitcnt lgkmcnt(8)
	v_mfma_f32_32x32x16_f16 v[240:255], v[144:147], v[40:43], v[240:255]
	s_waitcnt lgkmcnt(7)
	v_mfma_f32_32x32x16_f16 v[88:103], v[132:135], v[52:55], v[88:103]
	ds_read_b128 v[52:55], v205 offset:52800
	ds_read_b128 v[48:51], v207 offset:52800
	s_waitcnt lgkmcnt(8)
	v_mfma_f32_32x32x16_f16 v[88:103], v[108:111], v[82:85], v[88:103]
	s_and_saveexec_b64 s[2:3], s[0:1]
	s_cbranch_execz .LBB2_124
	ds_write_b128 v210, v[28:31] offset:16
	ds_write_b32 v233, v71 offset:548
	ds_write_b32 v234, v71 offset:536
	ds_write_b32 v235, v71 offset:560
.LBB2_124:
	s_or_b64 exec, exec, s[2:3]
	s_waitcnt lgkmcnt(7)
	v_mfma_f32_32x32x16_f16 v[88:103], v[128:131], v[66:69], v[88:103]
	ds_read_b128 v[40:43], v205 offset:53856
	ds_read_b128 v[28:31], v207 offset:53856
	v_mfma_f32_32x32x16_f16 v[240:255], v[132:135], v[66:69], v[240:255]
	s_waitcnt lgkmcnt(8)
	v_mfma_f32_32x32x16_f16 v[88:103], v[124:127], v[44:47], v[88:103]
	v_mfma_f32_32x32x16_f16 v[240:255], v[108:111], v[44:47], v[240:255]
	s_waitcnt lgkmcnt(7)
	v_mfma_f32_32x32x16_f16 v[88:103], v[116:119], v[52:55], v[88:103]
	v_mfma_f32_32x32x16_f16 v[240:255], v[128:131], v[52:55], v[240:255]
	s_waitcnt lgkmcnt(6)
	v_mfma_f32_32x32x16_f16 v[88:103], v[112:115], v[48:51], v[88:103]
	v_mfma_f32_32x32x16_f16 v[240:255], v[124:127], v[48:51], v[240:255]
	s_and_saveexec_b64 s[2:3], s[8:9]
	s_cbranch_execz .LBB2_129
	ds_write_b128 v211, v[24:27] offset:16
	ds_write_b32 v236, v87 offset:548
	ds_write_b32 v237, v87 offset:536
	ds_write_b32 v238, v87 offset:560

.LBB6_157:
	s_or_b64 exec, exec, s[50:51]
	s_waitcnt lgkmcnt(0)
	s_barrier
	ds_read_b128 v[26:29], v195
	ds_read_b128 v[50:53], v195 offset:1056
	ds_read_b128 v[54:57], v196
	ds_read_b128 v[154:157], v195 offset:2112
	ds_read_b128 v[158:161], v196 offset:1056
	ds_read_b128 v[162:165], v196 offset:2112
	s_waitcnt lgkmcnt(5)
	v_mfma_f32_32x32x16_f16 v[26:41], v[150:153], v[26:29], 0
	s_waitcnt lgkmcnt(3)
	v_mfma_f32_32x32x16_f16 v[26:41], v[146:149], v[54:57], v[26:41]
	v_mfma_f32_32x32x16_f16 v[26:41], v[142:145], v[50:53], v[26:41]
	ds_read_b128 v[50:53], v195 offset:3168
	ds_read_b128 v[54:57], v196 offset:3168
	s_waitcnt lgkmcnt(3)
	v_mfma_f32_32x32x16_f16 v[26:41], v[134:137], v[158:161], v[26:41]
	v_mfma_f32_32x32x16_f16 v[26:41], v[138:141], v[154:157], v[26:41]
	ds_read_b128 v[154:157], v195 offset:4224
	ds_read_b128 v[158:161], v196 offset:4224
	s_waitcnt lgkmcnt(4)
	v_mfma_f32_32x32x16_f16 v[26:41], v[130:133], v[162:165], v[26:41]
	s_waitcnt lgkmcnt(3)
	v_mfma_f32_32x32x16_f16 v[26:41], v[126:129], v[50:53], v[26:41]
	ds_read_b128 v[50:53], v195 offset:5280
	ds_read_b128 v[220:223], v196 offset:5280
	s_waitcnt lgkmcnt(4)
	v_mfma_f32_32x32x16_f16 v[26:41], v[118:121], v[54:57], v[26:41]
	s_waitcnt lgkmcnt(3)
	v_mfma_f32_32x32x16_f16 v[26:41], v[122:125], v[154:157], v[26:41]
	ds_read_b128 v[54:57], v195 offset:10560
	ds_read_b128 v[224:227], v196 offset:10560
	s_waitcnt lgkmcnt(4)
	v_mfma_f32_32x32x16_f16 v[26:41], v[110:113], v[158:161], v[26:41]
	s_waitcnt lgkmcnt(3)
	v_mfma_f32_32x32x16_f16 v[26:41], v[114:117], v[50:53], v[26:41]
	ds_read_b128 v[50:53], v195 offset:11616
	ds_read_b128 v[162:165], v196 offset:11616
	s_waitcnt lgkmcnt(4)
	v_mfma_f32_32x32x16_f16 v[26:41], v[102:105], v[220:223], v[26:41]
	s_waitcnt lgkmcnt(3)
	v_mfma_f32_32x32x16_f16 v[26:41], v[106:109], v[54:57], v[26:41]
	ds_read_b128 v[154:157], v195 offset:12672
	ds_read_b128 v[158:161], v196 offset:12672
	s_waitcnt lgkmcnt(4)
	v_mfma_f32_32x32x16_f16 v[26:41], v[98:101], v[224:227], v[26:41]
	s_and_saveexec_b64 s[50:51], s[12:13]
	s_cbranch_execz .LBB6_159
	ds_read2st64_b32 v[54:55], v199 offset1:1
	ds_read2st64_b32 v[220:221], v199 offset0:2 offset1:3
	v_add_co_u32_e32 v56, vcc, 0xffffd000, v176
	s_waitcnt lgkmcnt(1)
	v_add_f32_e32 v54, v170, v54
	v_add_f32_e32 v54, s61, v54
	v_max_f32_e32 v54, 0, v54
	v_add_f32_e32 v54, 0, v54
	v_addc_co_u32_e32 v57, vcc, -1, v177, vcc
	global_store_dword v[56:57], v54, off offset:-128
	v_add_f32_e32 v54, v209, v55
	v_add_f32_e32 v54, s61, v54
	v_max_f32_e32 v54, 0, v54
	v_add_f32_e32 v56, 0, v54
	v_add_co_u32_e32 v54, vcc, 0xffffe000, v176
	s_nop 1
	v_addc_co_u32_e32 v55, vcc, -1, v177, vcc
	global_store_dword v[54:55], v56, off offset:-128
	s_waitcnt lgkmcnt(0)
	v_add_f32_e32 v54, v211, v220
	v_add_f32_e32 v54, s61, v54
	v_max_f32_e32 v54, 0, v54
	v_add_f32_e32 v56, 0, v54
	v_add_co_u32_e32 v54, vcc, 0xfffff000, v176
	s_nop 1
	v_addc_co_u32_e32 v55, vcc, -1, v177, vcc
	global_store_dword v[54:55], v56, off offset:-128
	v_add_f32_e32 v54, v210, v221
	v_add_f32_e32 v54, s61, v54
	v_max_f32_e32 v54, 0, v54
	v_add_f32_e32 v54, 0, v54
	global_store_dword v[176:177], v54, off offset:-128

.LBB6_213:
	s_or_b64 exec, exec, s[16:17]
	v_add_f32_e32 v212, v17, v33
	v_mov_b32_e32 v17, v15
	v_mov_b32_e32 v33, v31
	v_pk_add_f32 v[166:167], v[16:17], v[32:33]
	v_lshl_add_u64 v[176:177], v[176:177], 0, s[42:43]
	v_add_u32_e32 v204, 64, v204
	v_add_u32_e32 v205, 64, v205
	v_add_u32_e32 v207, 64, v207
	s_cmp_gt_u32 s63, 13
	v_add_u32_e32 v208, 64, v208
	s_cbranch_scc1 .LBB6_215
	v_mov_b32_e32 v4, v28
	v_mov_b32_e32 v2, v26
	v_mov_b64_e32 v[14:15], v[38:39]
	v_mov_b64_e32 v[16:17], v[40:41]
	v_mov_b64_e32 v[18:19], v[42:43]
	v_mov_b64_e32 v[20:21], v[44:45]
	v_mov_b64_e32 v[22:23], v[46:47]
	v_mov_b64_e32 v[24:25], v[48:49]
	v_mov_b64_e32 v[26:27], v[50:51]
	v_mov_b64_e32 v[28:29], v[52:53]
	s_branch .LBB6_149
.LBB6_215:
	s_waitcnt lgkmcnt(0)
	s_barrier
	ds_read_b128 v[6:9], v195
	ds_read_b128 v[22:25], v195 offset:1056
	ds_read_b128 v[30:33], v196
	ds_read_b128 v[34:37], v195 offset:2112
	ds_read_b128 v[50:53], v196 offset:1056
	ds_read_b128 v[54:57], v196 offset:2112
	v_add_u32_e32 v2, s57, v198
	v_or_b32_e32 v2, v2, v190
	s_waitcnt lgkmcnt(5)
	v_mfma_f32_32x32x16_f16 v[6:21], v[150:153], v[6:9], 0
	v_lshl_add_u32 v2, v2, 5, s62
	v_or3_b32 v2, v2, v197, s58
	v_lshlrev_b32_e32 v2, 10, v2
	v_or_b32_e32 v150, v2, v206
	v_mov_b32_e32 v151, 0
	s_waitcnt lgkmcnt(3)
	v_mfma_f32_32x32x16_f16 v[6:21], v[146:149], v[30:33], v[6:21]
	v_mfma_f32_32x32x16_f16 v[6:21], v[142:145], v[22:25], v[6:21]
	ds_read_b128 v[22:25], v195 offset:3168
	ds_read_b128 v[30:33], v196 offset:3168
	s_waitcnt lgkmcnt(3)
	v_mfma_f32_32x32x16_f16 v[6:21], v[134:137], v[50:53], v[6:21]
	v_mfma_f32_32x32x16_f16 v[6:21], v[138:141], v[34:37], v[6:21]
	ds_read_b128 v[34:37], v195 offset:4224
	ds_read_b128 v[50:53], v196 offset:4224
	s_waitcnt lgkmcnt(4)
	v_mfma_f32_32x32x16_f16 v[6:21], v[130:133], v[54:57], v[6:21]
	s_waitcnt lgkmcnt(3)
	v_mfma_f32_32x32x16_f16 v[6:21], v[126:129], v[22:25], v[6:21]
	ds_read_b128 v[22:25], v195 offset:5280
	ds_read_b128 v[54:57], v196 offset:5280
	s_waitcnt lgkmcnt(4)
	v_mfma_f32_32x32x16_f16 v[6:21], v[118:121], v[30:33], v[6:21]
	s_waitcnt lgkmcnt(3)
	v_mfma_f32_32x32x16_f16 v[6:21], v[122:125], v[34:37], v[6:21]
	ds_read_b128 v[118:121], v195 offset:10560
	ds_read_b128 v[122:125], v196 offset:10560
	s_waitcnt lgkmcnt(4)
	v_mfma_f32_32x32x16_f16 v[6:21], v[110:113], v[50:53], v[6:21]
	s_waitcnt lgkmcnt(3)
	v_mfma_f32_32x32x16_f16 v[6:21], v[114:117], v[22:25], v[6:21]
	ds_read_b128 v[34:37], v195 offset:11616
	ds_read_b128 v[30:33], v196 offset:11616
	s_waitcnt lgkmcnt(4)
	v_mfma_f32_32x32x16_f16 v[6:21], v[102:105], v[54:57], v[6:21]
	s_waitcnt lgkmcnt(3)
	v_mfma_f32_32x32x16_f16 v[6:21], v[106:109], v[118:121], v[6:21]
	ds_read_b128 v[50:53], v195 offset:12672
	ds_read_b128 v[22:25], v196 offset:12672
	s_waitcnt lgkmcnt(4)
	v_mfma_f32_32x32x16_f16 v[6:21], v[98:101], v[122:125], v[6:21]
	s_and_saveexec_b64 s[4:5], s[12:13]
	s_cbranch_execz .LBB6_217
	ds_read2st64_b32 v[54:55], v199 offset1:1
	ds_read2st64_b32 v[98:99], v199 offset0:2 offset1:3
	v_lshl_add_u64 v[56:57], v[150:151], 2, s[28:29]
	s_waitcnt lgkmcnt(1)
	v_add_f32_e32 v4, v170, v54
	v_add_f32_e32 v4, s61, v4
	v_add_f32_e32 v27, v209, v55
	v_max_f32_e32 v4, 0, v4
	v_add_f32_e32 v27, s61, v27
	v_add_f32_e32 v4, 0, v4
	global_store_dword v[56:57], v4, off offset:3584
	v_max_f32_e32 v4, 0, v27
	v_add_co_u32_e32 v54, vcc, 0x1000, v56
	v_add_f32_e32 v4, 0, v4
	s_nop 0
	v_addc_co_u32_e32 v55, vcc, 0, v57, vcc
	global_store_dword v[54:55], v4, off offset:3584
	s_waitcnt lgkmcnt(0)
	v_add_f32_e32 v4, v211, v98
	v_add_f32_e32 v4, s61, v4
	v_max_f32_e32 v4, 0, v4
	v_add_co_u32_e32 v54, vcc, 0x2000, v56
	v_add_f32_e32 v4, 0, v4
	s_nop 0
	v_addc_co_u32_e32 v55, vcc, 0, v57, vcc
	global_store_dword v[54:55], v4, off offset:3584
	v_add_f32_e32 v4, v210, v99
	v_add_f32_e32 v4, s61, v4
	v_max_f32_e32 v4, 0, v4
	v_add_co_u32_e32 v54, vcc, 0x3000, v56
	v_add_f32_e32 v4, 0, v4
	s_nop 0
	v_addc_co_u32_e32 v55, vcc, 0, v57, vcc
	global_store_dword v[54:55], v4, off offset:3584

.LBB6_363:
	s_or_b64 exec, exec, s[40:41]
	s_waitcnt lgkmcnt(0)
	s_barrier
	ds_read_b128 v[26:29], v195
	ds_read_b128 v[42:45], v195 offset:1056
	ds_read_b128 v[46:49], v197
	ds_read_b128 v[50:53], v195 offset:2112
	ds_read_b128 v[158:161], v197 offset:1056
	ds_read_b128 v[162:165], v197 offset:2112
	s_waitcnt lgkmcnt(5)
	v_mfma_f32_32x32x16_f16 v[26:41], v[54:57], v[26:29], 0
	s_waitcnt lgkmcnt(3)
	v_mfma_f32_32x32x16_f16 v[26:41], v[58:61], v[46:49], v[26:41]
	v_mfma_f32_32x32x16_f16 v[26:41], v[62:65], v[42:45], v[26:41]
	ds_read_b128 v[42:45], v195 offset:3168
	ds_read_b128 v[46:49], v197 offset:3168
	s_waitcnt lgkmcnt(3)
	v_mfma_f32_32x32x16_f16 v[26:41], v[66:69], v[158:161], v[26:41]
	v_mfma_f32_32x32x16_f16 v[26:41], v[70:73], v[50:53], v[26:41]
	ds_read_b128 v[50:53], v195 offset:4224
	ds_read_b128 v[158:161], v197 offset:4224
	s_waitcnt lgkmcnt(4)
	v_mfma_f32_32x32x16_f16 v[26:41], v[74:77], v[162:165], v[26:41]
	s_waitcnt lgkmcnt(3)
	v_mfma_f32_32x32x16_f16 v[26:41], v[78:81], v[42:45], v[26:41]
	ds_read_b128 v[42:45], v195 offset:5280
	ds_read_b128 v[162:165], v197 offset:5280
	s_waitcnt lgkmcnt(4)
	v_mfma_f32_32x32x16_f16 v[26:41], v[82:85], v[46:49], v[26:41]
	s_waitcnt lgkmcnt(3)
	v_mfma_f32_32x32x16_f16 v[26:41], v[86:89], v[50:53], v[26:41]
	ds_read_b128 v[46:49], v195 offset:10560
	ds_read_b128 v[210:213], v197 offset:10560
	s_waitcnt lgkmcnt(4)
	v_mfma_f32_32x32x16_f16 v[26:41], v[90:93], v[158:161], v[26:41]
	s_waitcnt lgkmcnt(3)
	v_mfma_f32_32x32x16_f16 v[26:41], v[94:97], v[42:45], v[26:41]
	ds_read_b128 v[42:45], v195 offset:11616
	ds_read_b128 v[50:53], v197 offset:11616
	s_waitcnt lgkmcnt(4)
	v_mfma_f32_32x32x16_f16 v[26:41], v[98:101], v[162:165], v[26:41]
	s_waitcnt lgkmcnt(3)
	v_mfma_f32_32x32x16_f16 v[26:41], v[102:105], v[46:49], v[26:41]
	ds_read_b128 v[46:49], v195 offset:12672
	ds_read_b128 v[162:165], v197 offset:12672
	s_waitcnt lgkmcnt(4)
	v_mfma_f32_32x32x16_f16 v[26:41], v[106:109], v[210:213], v[26:41]
	s_and_saveexec_b64 s[40:41], s[12:13]
	s_cbranch_execz .LBB6_365
	ds_read2st64_b32 v[158:159], v185 offset1:1
	ds_read2st64_b32 v[168:169], v185 offset0:2 offset1:3
	v_lshl_add_u64 v[160:161], s[30:31], 0, v[178:179]
	s_waitcnt lgkmcnt(1)
	v_add_f32_e32 v158, v170, v158
	v_add_f32_e32 v158, s52, v158
	v_add_f32_e32 v159, v205, v159
	v_max_f32_e32 v158, 0, v158
	v_add_f32_e32 v159, s52, v159
	v_add_f32_e32 v158, 0, v158
	global_store_dword v[160:161], v158, off
	v_max_f32_e32 v158, 0, v159
	v_add_f32_e32 v170, 0, v158
	v_add_co_u32_e32 v158, vcc, 0x1000, v160
	s_nop 1
	v_addc_co_u32_e32 v159, vcc, 0, v161, vcc
	global_store_dword v[158:159], v170, off
	s_waitcnt lgkmcnt(0)
	v_add_f32_e32 v158, v208, v168
	v_add_f32_e32 v158, s52, v158
	v_max_f32_e32 v158, 0, v158
	v_add_f32_e32 v168, 0, v158
	v_add_co_u32_e32 v158, vcc, 0x2000, v160
	s_nop 1
	v_addc_co_u32_e32 v159, vcc, 0, v161, vcc
	global_store_dword v[158:159], v168, off
	v_add_f32_e32 v158, v207, v169
	v_add_f32_e32 v158, s52, v158
	v_max_f32_e32 v158, 0, v158
	v_add_f32_e32 v168, 0, v158
	v_add_co_u32_e32 v158, vcc, 0x3000, v160
	s_nop 1
	v_addc_co_u32_e32 v159, vcc, 0, v161, vcc
	global_store_dword v[158:159], v168, off

.LBB6_425:
	s_or_b64 exec, exec, s[16:17]
	v_add_f32_e32 v209, v17, v33
	v_mov_b32_e32 v17, v15
	v_mov_b32_e32 v33, v31
	v_pk_add_f32 v[166:167], v[16:17], v[32:33]
	s_add_u32 s30, s30, 0x100
	s_addc_u32 s31, s31, 0
	v_add_u32_e32 v183, 64, v183
	v_add_u32_e32 v184, 64, v184
	v_add_u32_e32 v201, 64, v201
	s_cmp_gt_u32 s54, 15
	v_add_u32_e32 v200, 64, v200
	s_cbranch_scc1 .LBB6_428
	v_mov_b32_e32 v4, v28
	v_mov_b32_e32 v2, v26
	v_mov_b64_e32 v[14:15], v[38:39]
	v_mov_b64_e32 v[16:17], v[40:41]
	v_mov_b64_e32 v[18:19], v[42:43]
	v_mov_b64_e32 v[20:21], v[44:45]
	v_mov_b64_e32 v[22:23], v[46:47]
	v_mov_b64_e32 v[24:25], v[48:49]
	v_mov_b64_e32 v[26:27], v[50:51]
	v_mov_b64_e32 v[28:29], v[52:53]
	s_branch .LBB6_355

.LBB6_428:
	s_waitcnt lgkmcnt(0)
	s_barrier
	v_add_u32_e32 v1, s57, v192
	v_or_b32_e32 v1, v1, v190
	v_lshl_add_u32 v1, v1, 5, s53
	v_or3_b32 v1, v1, v193, s58
	v_lshlrev_b32_e32 v1, 10, v1
	v_or_b32_e32 v2, v206, v1
	s_and_saveexec_b64 s[4:5], s[12:13]
	s_cbranch_execz .LBB6_430
	ds_read2st64_b32 v[4:5], v185 offset1:1
	ds_read2st64_b32 v[6:7], v185 offset0:2 offset1:3
	v_mov_b32_e32 v3, 0
	v_lshl_add_u64 v[8:9], v[2:3], 2, s[28:29]
	s_waitcnt lgkmcnt(1)
	v_add_f32_e32 v1, v170, v4
	v_add_f32_e32 v1, s52, v1
	v_max_f32_e32 v1, 0, v1
	v_add_f32_e32 v3, v205, v5
	v_add_f32_e32 v1, 0, v1
	global_store_dword v[8:9], v1, off offset:1792
	v_add_f32_e32 v1, s52, v3
	v_max_f32_e32 v1, 0, v1
	v_add_co_u32_e32 v4, vcc, 0x1000, v8
	v_add_f32_e32 v1, 0, v1
	s_nop 0
	v_addc_co_u32_e32 v5, vcc, 0, v9, vcc
	global_store_dword v[4:5], v1, off offset:1792
	s_waitcnt lgkmcnt(0)
	v_add_f32_e32 v1, v208, v6
	v_add_f32_e32 v1, s52, v1
	v_max_f32_e32 v1, 0, v1
	v_add_co_u32_e32 v4, vcc, 0x2000, v8
	v_add_f32_e32 v1, 0, v1
	s_nop 0
	v_addc_co_u32_e32 v5, vcc, 0, v9, vcc
	global_store_dword v[4:5], v1, off offset:1792
	v_add_f32_e32 v1, v207, v7
	v_add_f32_e32 v1, s52, v1
	v_max_f32_e32 v1, 0, v1
	v_add_co_u32_e32 v4, vcc, 0x3000, v8
	v_add_f32_e32 v1, 0, v1
	s_nop 0
	v_addc_co_u32_e32 v5, vcc, 0, v9, vcc
	global_store_dword v[4:5], v1, off offset:1792

.LBB6_532:
	s_or_b64 exec, exec, s[34:35]
	v_mfma_f32_32x32x16_f16 v[56:71], v[164:167], v[72:75], v[56:71]
	ds_read_b128 v[218:221], v209 offset:3168
	ds_read_b128 v[222:225], v211 offset:3168
	v_mfma_f32_32x32x16_f16 v[72:87], v[176:179], v[72:75], 0
	s_waitcnt lgkmcnt(3)
	v_mfma_f32_32x32x16_f16 v[56:71], v[160:163], v[100:103], v[56:71]
	v_mfma_f32_32x32x16_f16 v[72:87], v[172:175], v[100:103], v[72:87]
	v_mfma_f32_32x32x16_f16 v[56:71], v[168:171], v[96:99], v[56:71]
	v_mfma_f32_32x32x16_f16 v[72:87], v[164:167], v[96:99], v[72:87]
	ds_read_b128 v[96:99], v209 offset:6336
	ds_read_b128 v[100:103], v211 offset:6336
	s_waitcnt lgkmcnt(4)
	v_mfma_f32_32x32x16_f16 v[56:71], v[156:159], v[92:95], v[56:71]
	v_mfma_f32_32x32x16_f16 v[72:87], v[160:163], v[92:95], v[72:87]
	v_add_f32_e32 v14, v187, v14
	v_add_f32_e32 v15, v188, v15
	s_waitcnt lgkmcnt(3)
	v_mfma_f32_32x32x16_f16 v[72:87], v[168:171], v[218:221], v[72:87]
	v_add_f32_e32 v12, v180, v12
	v_add_f32_e32 v13, v186, v13
	v_max_f32_e32 v14, 0, v14
	v_max_f32_e32 v15, 0, v15
	v_max_f32_e32 v12, 0, v12
	v_max_f32_e32 v13, 0, v13
	v_cvt_pk_f16_f32 v15, v14, v15
	v_cvt_pk_f16_f32 v14, v12, v13
	v_add_f32_e32 v12, v189, v16
	v_max_f32_e32 v16, 0, v12
	v_add_f32_e32 v12, v184, v46
	v_add_f32_e32 v13, v185, v47
	v_max_f32_e32 v12, 0, v12
	v_max_f32_e32 v13, 0, v13
	s_waitcnt lgkmcnt(2)
	v_mfma_f32_32x32x16_f16 v[72:87], v[156:159], v[222:225], v[72:87]
	v_cvt_pk_f16_f32 v13, v12, v13
	v_add_f32_e32 v12, v182, v44
	v_add_f32_e32 v44, v183, v45
	v_max_f32_e32 v12, 0, v12
	v_max_f32_e32 v44, 0, v44
	ds_read_b128 v[92:95], v209 offset:7392
	ds_read_b128 v[226:229], v211 offset:7392
	v_cvt_pk_f16_f32 v12, v12, v44
	v_add_f32_e32 v44, v181, v48
	v_max_f32_e32 v46, 0, v44
	v_permlane32_swap_b32_e32 v12, v14
	v_permlane32_swap_b32_e32 v13, v15
	v_permlane32_swap_b32_e32 v46, v16
	v_lshl_add_u64 v[44:45], s[20:21], 0, v[200:201]
	global_store_dwordx4 v[44:45], v[12:15], off sc1
	s_nop 1
	v_cvt_pk_f16_f32 v12, v46, v16
	global_store_dword v[198:199], v12, off sc1
	s_waitcnt lgkmcnt(3)
	v_mfma_f32_32x32x16_f16 v[56:71], v[132:135], v[96:99], v[56:71]
	ds_read_b128 v[96:99], v209 offset:8448
	ds_read_b128 v[180:183], v211 offset:8448
	s_waitcnt lgkmcnt(4)
	v_mfma_f32_32x32x16_f16 v[56:71], v[140:143], v[100:103], v[56:71]
	s_waitcnt lgkmcnt(3)
	v_mfma_f32_32x32x16_f16 v[56:71], v[120:123], v[92:95], v[56:71]
	ds_read_b128 v[12:15], v209 offset:9504
	ds_read_b128 v[44:47], v211 offset:9504
	v_mfma_f32_32x32x16_f16 v[72:87], v[132:135], v[92:95], v[72:87]
	s_waitcnt lgkmcnt(4)
	v_mfma_f32_32x32x16_f16 v[56:71], v[152:155], v[226:229], v[56:71]
	v_mfma_f32_32x32x16_f16 v[72:87], v[140:143], v[226:229], v[72:87]
	s_waitcnt lgkmcnt(3)
	v_mfma_f32_32x32x16_f16 v[56:71], v[148:151], v[96:99], v[56:71]
	v_mfma_f32_32x32x16_f16 v[72:87], v[120:123], v[96:99], v[72:87]
	ds_read_b128 v[100:103], v209 offset:12672
	ds_read_b128 v[96:99], v211 offset:12672
	s_waitcnt vmcnt(3)
	ds_write_b128 v212, v[88:91] offset:38032
	s_waitcnt vmcnt(2)
	ds_write_b32 v230, v49 offset:38564
	s_waitcnt lgkmcnt(6)
	v_mfma_f32_32x32x16_f16 v[56:71], v[144:147], v[180:183], v[56:71]
	v_mfma_f32_32x32x16_f16 v[72:87], v[152:155], v[180:183], v[72:87]
	ds_write_b32 v231, v49 offset:38552
	ds_write_b32 v232, v49 offset:38576
	s_waitcnt lgkmcnt(7)
	v_mfma_f32_32x32x16_f16 v[72:87], v[148:151], v[12:15], v[72:87]
	ds_read_b128 v[92:95], v209 offset:13728
	ds_read_b128 v[12:15], v211 offset:13728
	s_waitcnt lgkmcnt(8)
	v_mfma_f32_32x32x16_f16 v[72:87], v[144:147], v[44:47], v[72:87]
	s_waitcnt lgkmcnt(7)
	v_mfma_f32_32x32x16_f16 v[56:71], v[136:139], v[100:103], v[56:71]
	ds_read_b128 v[88:91], v209 offset:14784
	ds_read_b128 v[44:47], v211 offset:14784
	s_waitcnt lgkmcnt(8)
	v_mfma_f32_32x32x16_f16 v[56:71], v[108:111], v[96:99], v[56:71]
	s_and_saveexec_b64 s[34:35], s[0:1]
	s_cbranch_execz .LBB6_541
	ds_write_b128 v214, v[28:31] offset:38032
	ds_write_b32 v233, v23 offset:38564
	ds_write_b32 v234, v23 offset:38552
	ds_write_b32 v235, v23 offset:38576
.LBB6_541:
	s_or_b64 exec, exec, s[34:35]
	s_waitcnt lgkmcnt(7)
	v_mfma_f32_32x32x16_f16 v[56:71], v[128:131], v[92:95], v[56:71]
	v_mfma_f32_32x32x16_f16 v[72:87], v[136:139], v[92:95], v[72:87]
	ds_read_b128 v[92:95], v209 offset:15840
	ds_read_b128 v[28:31], v211 offset:15840
	s_waitcnt lgkmcnt(8)
	v_mfma_f32_32x32x16_f16 v[56:71], v[124:127], v[12:15], v[56:71]
	v_mfma_f32_32x32x16_f16 v[72:87], v[108:111], v[12:15], v[72:87]
	s_waitcnt lgkmcnt(15)
	s_and_saveexec_b64 s[34:35], s[8:9]
	s_cbranch_execz .LBB6_546
	ds_write_b128 v215, v[24:27] offset:38032
	ds_write_b32 v236, v17 offset:38564
	ds_write_b32 v237, v17 offset:38552
	ds_write_b32 v238, v17 offset:38576

.LBB6_552:
	s_or_b64 exec, exec, s[28:29]
	v_add_f32_e32 v39, v18, v39
	v_add_f32_e32 v202, v19, v40
	v_add_f32_e32 v203, v20, v41
	v_add_f32_e32 v204, v21, v42
	v_add_f32_e32 v205, v22, v43
	v_add_f32_e32 v7, v50, v7
	v_add_f32_e32 v218, v51, v8
	v_add_f32_e32 v219, v52, v9
	v_add_f32_e32 v220, v53, v10
	v_add_f32_e32 v221, v54, v11
	v_mfma_f32_32x32x16_f16 v[88:103], v[164:167], v[12:15], v[88:103]
	ds_read_b128 v[40:43], v209 offset:41184
	ds_read_b128 v[48:51], v211 offset:41184
	v_mfma_f32_32x32x16_f16 v[240:255], v[176:179], v[12:15], 0
	s_waitcnt lgkmcnt(3)
	v_mfma_f32_32x32x16_f16 v[88:103], v[160:163], v[188:191], v[88:103]
	v_mfma_f32_32x32x16_f16 v[240:255], v[172:175], v[188:191], v[240:255]
	v_mfma_f32_32x32x16_f16 v[88:103], v[168:171], v[184:187], v[88:103]
	v_mfma_f32_32x32x16_f16 v[240:255], v[164:167], v[184:187], v[240:255]
	ds_read_b128 v[52:55], v209 offset:44352
	ds_read_b128 v[184:187], v211 offset:44352
	s_waitcnt lgkmcnt(4)
	v_mfma_f32_32x32x16_f16 v[88:103], v[156:159], v[180:183], v[88:103]
	v_mfma_f32_32x32x16_f16 v[240:255], v[160:163], v[180:183], v[240:255]
	v_add_f32_e32 v84, v219, v84
	v_add_f32_e32 v85, v220, v85
	s_waitcnt lgkmcnt(3)
	v_mfma_f32_32x32x16_f16 v[240:255], v[168:171], v[40:43], v[240:255]
	v_add_f32_e32 v40, 0, v85
	v_max_f32_e32 v84, 0, v84
	v_max_f32_e32 v40, 0, v40
	v_cvt_pk_f16_f32 v43, v84, v40
	v_add_f32_e32 v7, v7, v82
	v_add_f32_e32 v40, v218, v83
	v_max_f32_e32 v7, 0, v7
	v_max_f32_e32 v40, 0, v40
	v_cvt_pk_f16_f32 v42, v7, v40
	v_add_f32_e32 v40, v203, v68
	v_add_f32_e32 v41, v204, v69
	v_max_f32_e32 v40, 0, v40
	v_max_f32_e32 v41, 0, v41
	s_waitcnt lgkmcnt(2)
	v_mfma_f32_32x32x16_f16 v[240:255], v[156:159], v[48:51], v[240:255]
	v_cvt_pk_f16_f32 v41, v40, v41
	v_add_f32_e32 v39, v39, v66
	v_add_f32_e32 v40, v202, v67
	v_max_f32_e32 v39, 0, v39
	v_max_f32_e32 v40, 0, v40
	ds_read_b128 v[180:183], v209 offset:45408
	ds_read_b128 v[188:191], v211 offset:45408
	v_add_f32_e32 v7, v221, v86
	v_cvt_pk_f16_f32 v40, v39, v40
	v_add_f32_e32 v39, v205, v70
	v_max_f32_e32 v7, 0, v7
	v_max_f32_e32 v39, 0, v39
	s_nop 1
	v_permlane32_swap_b32_e32 v39, v7
	v_permlane32_swap_b32_e32 v40, v42
	v_permlane32_swap_b32_e32 v41, v43
	v_lshl_add_u64 v[48:49], s[20:21], 0, v[194:195]
	v_cvt_pk_f16_f32 v7, v39, v7
	global_store_dwordx4 v[48:49], v[40:43], off offset:1024 sc1
	global_store_dword v[196:197], v7, off sc1
	s_waitcnt lgkmcnt(3)
	v_mfma_f32_32x32x16_f16 v[88:103], v[132:135], v[52:55], v[88:103]
	ds_read_b128 v[52:55], v209 offset:46464
	ds_read_b128 v[66:69], v211 offset:46464
	s_waitcnt lgkmcnt(4)
	v_mfma_f32_32x32x16_f16 v[88:103], v[140:143], v[184:187], v[88:103]
	s_waitcnt lgkmcnt(3)
	v_mfma_f32_32x32x16_f16 v[88:103], v[120:123], v[180:183], v[88:103]
	ds_read_b128 v[48:51], v209 offset:47520
	ds_read_b128 v[40:43], v211 offset:47520
	v_mfma_f32_32x32x16_f16 v[240:255], v[132:135], v[180:183], v[240:255]
	s_waitcnt lgkmcnt(4)
	v_mfma_f32_32x32x16_f16 v[88:103], v[152:155], v[188:191], v[88:103]
	v_mfma_f32_32x32x16_f16 v[240:255], v[140:143], v[188:191], v[240:255]
	s_waitcnt lgkmcnt(3)
	v_mfma_f32_32x32x16_f16 v[88:103], v[148:151], v[52:55], v[88:103]
	v_mfma_f32_32x32x16_f16 v[240:255], v[120:123], v[52:55], v[240:255]
	ds_read_b128 v[52:55], v209 offset:50688
	ds_read_b128 v[82:85], v211 offset:50688
	s_waitcnt vmcnt(3)
	ds_write_b128 v212, v[44:47] offset:16
	s_waitcnt vmcnt(2)
	ds_write_b32 v230, v87 offset:548
	s_waitcnt lgkmcnt(6)
	v_mfma_f32_32x32x16_f16 v[88:103], v[144:147], v[66:69], v[88:103]
	v_mfma_f32_32x32x16_f16 v[240:255], v[152:155], v[66:69], v[240:255]
	ds_write_b32 v231, v87 offset:536
	ds_write_b32 v232, v87 offset:560
	s_waitcnt lgkmcnt(7)
	v_mfma_f32_32x32x16_f16 v[240:255], v[148:151], v[48:51], v[240:255]
	ds_read_b128 v[66:69], v209 offset:51744
	ds_read_b128 v[44:47], v211 offset:51744
	s_waitcnt lgkmcnt(8)
	v_mfma_f32_32x32x16_f16 v[240:255], v[144:147], v[40:43], v[240:255]
	s_waitcnt lgkmcnt(7)
	v_mfma_f32_32x32x16_f16 v[88:103], v[136:139], v[52:55], v[88:103]
	ds_read_b128 v[52:55], v209 offset:52800
	ds_read_b128 v[48:51], v211 offset:52800
	s_waitcnt lgkmcnt(8)
	v_mfma_f32_32x32x16_f16 v[88:103], v[108:111], v[82:85], v[88:103]
	s_and_saveexec_b64 s[2:3], s[0:1]
	s_cbranch_execz .LBB6_561
	ds_write_b128 v214, v[28:31] offset:16
	ds_write_b32 v233, v71 offset:548
	ds_write_b32 v234, v71 offset:536
	ds_write_b32 v235, v71 offset:560
.LBB6_561:
	s_or_b64 exec, exec, s[2:3]
	s_waitcnt lgkmcnt(7)
	v_mfma_f32_32x32x16_f16 v[88:103], v[128:131], v[66:69], v[88:103]
	ds_read_b128 v[40:43], v209 offset:53856
	ds_read_b128 v[28:31], v211 offset:53856
	v_mfma_f32_32x32x16_f16 v[240:255], v[136:139], v[66:69], v[240:255]
	s_waitcnt lgkmcnt(8)
	v_mfma_f32_32x32x16_f16 v[88:103], v[124:127], v[44:47], v[88:103]
	v_mfma_f32_32x32x16_f16 v[240:255], v[108:111], v[44:47], v[240:255]
	s_waitcnt lgkmcnt(7)
	v_mfma_f32_32x32x16_f16 v[88:103], v[116:119], v[52:55], v[88:103]
	v_mfma_f32_32x32x16_f16 v[240:255], v[128:131], v[52:55], v[240:255]
	s_waitcnt lgkmcnt(6)
	v_mfma_f32_32x32x16_f16 v[88:103], v[112:115], v[48:51], v[88:103]
	v_mfma_f32_32x32x16_f16 v[240:255], v[124:127], v[48:51], v[240:255]
	s_and_saveexec_b64 s[2:3], s[8:9]
	s_cbranch_execz .LBB6_566
	ds_write_b128 v215, v[24:27] offset:16
	ds_write_b32 v236, v32 offset:548
	ds_write_b32 v237, v32 offset:536
	ds_write_b32 v238, v32 offset:560

.LBB8_154:
	s_or_b64 exec, exec, s[44:45]
	s_waitcnt lgkmcnt(0)
	s_barrier
	ds_read_b128 v[26:29], v204
	ds_read_b128 v[54:57], v204 offset:1056
	ds_read_b128 v[154:157], v205
	ds_read_b128 v[50:53], v205 offset:1056
	v_lshl_add_u64 v[184:185], v[174:175], 0, s[36:37]
	s_and_saveexec_b64 s[44:45], s[10:11]
	s_cbranch_execz .LBB8_156
	v_add_co_u32_e32 v30, vcc, 0x1000, v184
	s_nop 1
	v_addc_co_u32_e32 v31, vcc, 0, v185, vcc
	v_add_co_u32_e32 v32, vcc, 0x2000, v184
	s_nop 1
	v_addc_co_u32_e32 v33, vcc, 0, v185, vcc
	v_add_co_u32_e32 v34, vcc, 0x3000, v184
	s_nop 1
	v_addc_co_u32_e32 v35, vcc, 0, v185, vcc
	global_load_dword v213, v[184:185], off offset:2048
	global_load_dword v216, v[30:31], off offset:2048
	global_load_dword v215, v[32:33], off offset:2048
	global_load_dword v214, v[34:35], off offset:2048

.LBB8_214:
	s_or_b64 exec, exec, s[14:15]
	v_add_f32_e32 v224, v17, v33
	v_mov_b32_e32 v17, v15
	v_mov_b32_e32 v33, v31
	v_pk_add_f32 v[166:167], v[16:17], v[32:33]
	s_add_u32 s36, s36, 0x100
	s_addc_u32 s37, s37, 0
	v_add_u32_e32 v220, 64, v220
	v_add_u32_e32 v219, 64, v219
	v_add_u32_e32 v218, 64, v218
	s_cmp_gt_u32 s57, 13
	v_add_u32_e32 v217, 64, v217
	s_cbranch_scc1 .LBB8_216
	v_mov_b32_e32 v4, v28
	v_mov_b32_e32 v2, v26
	v_mov_b64_e32 v[14:15], v[38:39]
	v_mov_b64_e32 v[16:17], v[40:41]
	v_mov_b64_e32 v[18:19], v[42:43]
	v_mov_b64_e32 v[20:21], v[44:45]
	v_mov_b64_e32 v[22:23], v[46:47]
	v_mov_b64_e32 v[24:25], v[48:49]
	v_mov_b64_e32 v[26:27], v[50:51]
	v_mov_b64_e32 v[28:29], v[52:53]
	s_branch .LBB8_146
.LBB8_216:
	s_waitcnt lgkmcnt(0)
	s_barrier
	v_add_u32_e32 v1, s33, v208
	ds_read_b128 v[6:9], v204
	ds_read_b128 v[30:33], v204 offset:1056
	ds_read_b128 v[34:37], v205
	ds_read_b128 v[22:25], v205 offset:1056
	v_or_b32_e32 v1, v1, v191
	v_lshl_add_u32 v1, v1, 5, s56
	v_or3_b32 v1, v1, v207, s50
	v_lshlrev_b32_e32 v1, 10, v1
	v_or_b32_e32 v154, v1, v190
	v_ashrrev_i32_e32 v155, 31, v154
	s_and_saveexec_b64 s[2:3], s[10:11]
	s_cbranch_execz .LBB8_218
	v_lshl_add_u64 v[10:11], v[154:155], 2, s[24:25]
	v_add_co_u32_e32 v12, vcc, 0x1000, v10
	s_nop 1
	v_addc_co_u32_e32 v13, vcc, 0, v11, vcc
	v_add_co_u32_e32 v14, vcc, 0x2000, v10
	s_nop 1
	v_addc_co_u32_e32 v15, vcc, 0, v11, vcc
	v_add_co_u32_e32 v16, vcc, 0x3000, v10
	s_nop 1
	v_addc_co_u32_e32 v17, vcc, 0, v11, vcc
	global_load_dword v213, v[10:11], off offset:3584
	global_load_dword v216, v[12:13], off offset:3584
	global_load_dword v215, v[14:15], off offset:3584
	global_load_dword v214, v[16:17], off offset:3584

.LBB8_366:
	s_or_b64 exec, exec, s[34:35]
	s_waitcnt lgkmcnt(0)
	s_barrier
	ds_read_b128 v[24:27], v187
	ds_read_b128 v[44:47], v187 offset:1056
	ds_read_b128 v[48:51], v189
	ds_read_b128 v[40:43], v189 offset:1056
	v_add_u32_e32 v164, v190, v199
	v_ashrrev_i32_e32 v165, 31, v164
	v_add_u32_e32 v170, 0x400, v164
	v_add_u32_e32 v158, 0x800, v164
	v_add_u32_e32 v156, 0xc00, v164
	s_and_saveexec_b64 s[34:35], s[10:11]
	s_cbranch_execz .LBB8_368
	v_lshl_add_u64 v[28:29], v[164:165], 2, s[24:25]
	v_ashrrev_i32_e32 v171, 31, v170
	v_ashrrev_i32_e32 v159, 31, v158
	v_ashrrev_i32_e32 v157, 31, v156
	v_lshl_add_u64 v[30:31], v[170:171], 2, s[24:25]
	v_lshl_add_u64 v[32:33], v[158:159], 2, s[24:25]
	v_lshl_add_u64 v[34:35], v[156:157], 2, s[24:25]
	global_load_dword v203, v[28:29], off
	global_load_dword v204, v[30:31], off
	global_load_dword v205, v[32:33], off
	global_load_dword v206, v[34:35], off

.LBB8_432:
	s_or_b64 exec, exec, s[14:15]
	v_add_f32_e32 v179, v15, v31
	v_mov_b32_e32 v15, v13
	v_mov_b32_e32 v31, v29
	v_pk_add_f32 v[166:167], v[14:15], v[30:31]
	v_add_u32_e32 v199, 64, v199
	v_add_u32_e32 v194, 64, v194
	v_add_u32_e32 v201, 64, v201
	v_add_u32_e32 v193, 64, v193
	s_cmp_gt_u32 s48, 15
	v_add_u32_e32 v202, 64, v202
	s_cbranch_scc1 .LBB8_434
	v_mov_b32_e32 v2, v26
	v_mov_b32_e32 v0, v24
	v_mov_b64_e32 v[12:13], v[36:37]
	v_mov_b64_e32 v[14:15], v[38:39]
	v_mov_b64_e32 v[16:17], v[40:41]
	v_mov_b64_e32 v[18:19], v[42:43]
	v_mov_b64_e32 v[20:21], v[44:45]
	v_mov_b64_e32 v[22:23], v[46:47]
	v_mov_b64_e32 v[24:25], v[48:49]
	v_mov_b64_e32 v[26:27], v[50:51]
	s_branch .LBB8_358
.LBB8_434:
	s_waitcnt lgkmcnt(0)
	s_barrier
	v_add_u32_e32 v0, s33, v185
	v_or_b32_e32 v0, v0, v191
	v_lshl_add_u32 v0, v0, 5, s47
	v_or3_b32 v0, v0, v186, s50
	v_lshlrev_b32_e32 v0, 10, v0
	v_or_b32_e32 v0, v190, v0
	v_ashrrev_i32_e32 v1, 31, v0
	s_and_saveexec_b64 s[0:1], s[10:11]
	s_cbranch_execz .LBB8_436
	v_lshl_add_u64 v[2:3], v[0:1], 2, s[24:25]
	v_add_co_u32_e32 v4, vcc, 0x1000, v2
	s_nop 1
	v_addc_co_u32_e32 v5, vcc, 0, v3, vcc
	v_add_co_u32_e32 v6, vcc, 0x2000, v2
	s_nop 1
	v_addc_co_u32_e32 v7, vcc, 0, v3, vcc
	v_add_co_u32_e32 v8, vcc, 0x3000, v2
	global_load_dword v14, v[2:3], off offset:1792
	global_load_dword v15, v[4:5], off offset:1792
	global_load_dword v16, v[6:7], off offset:1792
	v_addc_co_u32_e32 v9, vcc, 0, v3, vcc
	global_load_dword v17, v[8:9], off offset:1792
	ds_read2st64_b32 v[10:11], v196 offset1:1
	ds_read2st64_b32 v[12:13], v196 offset0:2 offset1:3
	s_waitcnt lgkmcnt(1)
	v_add_f32_e32 v10, v168, v10
	v_add_f32_e32 v11, v176, v11
	v_add_f32_e32 v10, s46, v10
	s_waitcnt lgkmcnt(0)
	v_add_f32_e32 v12, v178, v12
	v_add_f32_e32 v11, s46, v11
	v_max_f32_e32 v10, 0, v10
	v_add_f32_e32 v13, v177, v13
	v_add_f32_e32 v12, s46, v12
	v_max_f32_e32 v11, 0, v11
	v_add_f32_e32 v13, s46, v13
	v_max_f32_e32 v12, 0, v12
	v_max_f32_e32 v13, 0, v13
	s_waitcnt vmcnt(3)
	v_add_f32_e32 v10, v14, v10
	global_store_dword v[2:3], v10, off offset:1792
	s_waitcnt vmcnt(3)
	v_add_f32_e32 v2, v15, v11
	global_store_dword v[4:5], v2, off offset:1792
	s_waitcnt vmcnt(3)
	v_add_f32_e32 v2, v16, v12
	global_store_dword v[6:7], v2, off offset:1792
	s_waitcnt vmcnt(3)
	v_add_f32_e32 v2, v17, v13
	global_store_dword v[8:9], v2, off offset:1792
